# strategy 7.11: K-loop back-edge rotated - counter/address SALU moved in front of the loop-back s_barrier in the six GEMM K-loops (exact reorder)
# speedup vs baseline: 1.0042x; 1.0042x over previous
.LBB0_285:
	ds_read_b128 v[18:21], v201
	ds_read_b128 v[22:25], v201 offset:1024
	ds_read_b128 v[26:29], v201 offset:2048
	ds_read_b128 v[30:33], v201 offset:3072
	ds_read_b128 v[2:5], v202
	ds_read_b128 v[6:9], v202 offset:1024
	ds_read_b128 v[10:13], v202 offset:2048
	ds_read_b128 v[14:17], v202 offset:3072
	s_add_u32 s62, s58, 0xfffc0080
	s_addc_u32 s63, s59, -1
	s_cmp_eq_u32 s71, 12
	s_cselect_b32 s67, s43, s63
	s_cselect_b32 s66, s57, s62
	s_cselect_b32 s63, s45, s70
	s_cselect_b32 s62, s68, s69
	v_lshl_add_u64 v[232:233], s[58:59], 0, v[172:173]
	s_add_i32 m0, s55, 0xc000
	ds_read_b128 v[176:179], v203
	ds_read_b128 v[180:183], v203 offset:1024
	ds_read_b128 v[206:209], v203 offset:2048
	ds_read_b128 v[210:213], v203 offset:3072
	ds_read_b128 v[214:217], v203 offset:4096
	ds_read_b128 v[218:221], v203 offset:5120
	ds_read_b128 v[222:225], v203 offset:6144
	ds_read_b128 v[226:229], v203 offset:7168
	global_load_lds_dwordx4 v[232:233], off
	v_lshl_add_u64 v[232:233], s[58:59], 0, v[174:175]
	s_add_i32 m0, s55, 0xe000
	s_nop 0
	global_load_lds_dwordx4 v[232:233], off
	s_waitcnt vmcnt(8)
	s_waitcnt lgkmcnt(0)
	s_barrier
	s_setprio 1
	s_waitcnt lgkmcnt(0)
	v_mfma_scale_f32_16x16x128_f8f6f4 v[158:161], v[18:25], v[176:183], v[158:161], v204, v204 op_sel_hi:[0,0,0]
	v_mfma_scale_f32_16x16x128_f8f6f4 v[154:157], v[26:33], v[176:183], v[154:157], v204, v204 op_sel_hi:[0,0,0]
	v_mfma_scale_f32_16x16x128_f8f6f4 v[150:153], v[18:25], v[206:213], v[150:153], v204, v204 op_sel_hi:[0,0,0]
	v_mfma_scale_f32_16x16x128_f8f6f4 v[146:149], v[26:33], v[206:213], v[146:149], v204, v204 op_sel_hi:[0,0,0]
	v_mfma_scale_f32_16x16x128_f8f6f4 v[130:133], v[18:25], v[214:221], v[130:133], v204, v204 op_sel_hi:[0,0,0]
	v_mfma_scale_f32_16x16x128_f8f6f4 v[122:125], v[26:33], v[214:221], v[122:125], v204, v204 op_sel_hi:[0,0,0]
	v_mfma_scale_f32_16x16x128_f8f6f4 v[118:121], v[18:25], v[222:229], v[118:121], v204, v204 op_sel_hi:[0,0,0]
	v_mfma_scale_f32_16x16x128_f8f6f4 v[114:117], v[26:33], v[222:229], v[114:117], v204, v204 op_sel_hi:[0,0,0]
	s_setprio 0
	s_setprio 1
	v_mfma_scale_f32_16x16x128_f8f6f4 v[142:145], v[2:9], v[176:183], v[142:145], v204, v204 op_sel_hi:[0,0,0]
	v_mfma_scale_f32_16x16x128_f8f6f4 v[138:141], v[10:17], v[176:183], v[138:141], v204, v204 op_sel_hi:[0,0,0]
	v_mfma_scale_f32_16x16x128_f8f6f4 v[134:137], v[2:9], v[206:213], v[134:137], v204, v204 op_sel_hi:[0,0,0]
	v_mfma_scale_f32_16x16x128_f8f6f4 v[126:129], v[10:17], v[206:213], v[126:129], v204, v204 op_sel_hi:[0,0,0]
	v_mfma_scale_f32_16x16x128_f8f6f4 v[110:113], v[2:9], v[214:221], v[110:113], v204, v204 op_sel_hi:[0,0,0]
	v_mfma_scale_f32_16x16x128_f8f6f4 v[106:109], v[10:17], v[214:221], v[106:109], v204, v204 op_sel_hi:[0,0,0]
	v_mfma_scale_f32_16x16x128_f8f6f4 v[102:105], v[2:9], v[222:229], v[102:105], v204, v204 op_sel_hi:[0,0,0]
	v_mfma_scale_f32_16x16x128_f8f6f4 v[98:101], v[10:17], v[222:229], v[98:101], v204, v204 op_sel_hi:[0,0,0]
	s_setprio 0
	s_barrier
	s_add_i32 vcc_lo, s97, s39
	v_lshl_add_u64 v[176:177], s[62:63], 0, v[164:165]
	s_mov_b32 m0, vcc_lo
	ds_read_b128 v[206:209], v203 offset:16384
	ds_read_b128 v[210:213], v203 offset:17408
	ds_read_b128 v[214:217], v203 offset:18432
	ds_read_b128 v[218:221], v203 offset:19456
	ds_read_b128 v[222:225], v203 offset:20480
	ds_read_b128 v[226:229], v203 offset:21504
	ds_read_b128 v[232:235], v203 offset:22528
	ds_read_b128 v[236:239], v203 offset:23552
	global_load_lds_dwordx4 v[176:177], off
	s_add_i32 m0, vcc_lo, 0x2000
	s_add_u32 vcc_lo, s62, 0x40000
	v_lshl_add_u64 v[178:179], s[62:63], 0, v[168:169]
	s_addc_u32 vcc_hi, s63, 0
	s_add_i32 s18, s34, s39
	global_load_lds_dwordx4 v[178:179], off
	v_lshl_add_u64 v[180:181], vcc, 0, v[164:165]
	s_mov_b32 m0, s18
	v_lshl_add_u64 v[182:183], s[66:67], 0, v[166:167]
	global_load_lds_dwordx4 v[180:181], off
	v_lshl_add_u64 v[180:181], vcc, 0, v[168:169]
	s_add_i32 m0, s18, 0x2000
	s_nop 0
	global_load_lds_dwordx4 v[180:181], off
	v_lshl_add_u64 v[180:181], s[66:67], 0, v[162:163]
	s_mov_b32 m0, s55
	s_nop 0
	global_load_lds_dwordx4 v[180:181], off
	s_mov_b32 m0, s90
	s_nop 0
	global_load_lds_dwordx4 v[182:183], off
	s_waitcnt vmcnt(8)
	s_waitcnt lgkmcnt(0)
	s_barrier
	s_setprio 1
	s_waitcnt lgkmcnt(0)
	v_mfma_scale_f32_16x16x128_f8f6f4 v[94:97], v[18:25], v[206:213], v[94:97], v204, v204 op_sel_hi:[0,0,0]
	v_mfma_scale_f32_16x16x128_f8f6f4 v[90:93], v[26:33], v[206:213], v[90:93], v204, v204 op_sel_hi:[0,0,0]
	v_mfma_scale_f32_16x16x128_f8f6f4 v[86:89], v[18:25], v[214:221], v[86:89], v204, v204 op_sel_hi:[0,0,0]
	v_mfma_scale_f32_16x16x128_f8f6f4 v[82:85], v[26:33], v[214:221], v[82:85], v204, v204 op_sel_hi:[0,0,0]
	v_mfma_scale_f32_16x16x128_f8f6f4 v[66:69], v[18:25], v[222:229], v[66:69], v204, v204 op_sel_hi:[0,0,0]
	v_mfma_scale_f32_16x16x128_f8f6f4 v[58:61], v[26:33], v[222:229], v[58:61], v204, v204 op_sel_hi:[0,0,0]
	v_mfma_scale_f32_16x16x128_f8f6f4 v[54:57], v[18:25], v[232:239], v[54:57], v204, v204 op_sel_hi:[0,0,0]
	v_mfma_scale_f32_16x16x128_f8f6f4 v[50:53], v[26:33], v[232:239], v[50:53], v204, v204 op_sel_hi:[0,0,0]
	s_setprio 0
	s_setprio 1
	v_mfma_scale_f32_16x16x128_f8f6f4 v[78:81], v[2:9], v[206:213], v[78:81], v204, v204 op_sel_hi:[0,0,0]
	v_mfma_scale_f32_16x16x128_f8f6f4 v[74:77], v[10:17], v[206:213], v[74:77], v204, v204 op_sel_hi:[0,0,0]
	v_mfma_scale_f32_16x16x128_f8f6f4 v[70:73], v[2:9], v[214:221], v[70:73], v204, v204 op_sel_hi:[0,0,0]
	v_mfma_scale_f32_16x16x128_f8f6f4 v[62:65], v[10:17], v[214:221], v[62:65], v204, v204 op_sel_hi:[0,0,0]
	v_mfma_scale_f32_16x16x128_f8f6f4 v[46:49], v[2:9], v[222:229], v[46:49], v204, v204 op_sel_hi:[0,0,0]
	v_mfma_scale_f32_16x16x128_f8f6f4 v[42:45], v[10:17], v[222:229], v[42:45], v204, v204 op_sel_hi:[0,0,0]
	v_mfma_scale_f32_16x16x128_f8f6f4 v[38:41], v[2:9], v[232:239], v[38:41], v204, v204 op_sel_hi:[0,0,0]
	v_mfma_scale_f32_16x16x128_f8f6f4 v[34:37], v[10:17], v[232:239], v[34:37], v204, v204 op_sel_hi:[0,0,0]
	s_setprio 0
	s_barrier
	s_add_i32 s18, 0, 0x18000
	s_add_i32 s19, 0, 0x1c000
	v_add_u32_e32 v14, s18, v198
	v_add_u32_e32 v30, s19, v198
	ds_read_b128 v[2:5], v14
	ds_read_b128 v[6:9], v14 offset:1024
	ds_read_b128 v[10:13], v14 offset:2048
	ds_read_b128 v[14:17], v14 offset:3072
	ds_read_b128 v[18:21], v30
	ds_read_b128 v[22:25], v30 offset:1024
	ds_read_b128 v[26:29], v30 offset:2048
	ds_read_b128 v[30:33], v30 offset:3072
	s_add_u32 s66, s66, 0x40000
	s_addc_u32 s67, s67, 0
	s_mov_b32 m0, s91
	v_lshl_add_u64 v[240:241], s[66:67], 0, v[162:163]
	ds_read_b128 v[206:209], v203 offset:32768
	ds_read_b128 v[210:213], v203 offset:33792
	ds_read_b128 v[214:217], v203 offset:34816
	ds_read_b128 v[218:221], v203 offset:35840
	ds_read_b128 v[222:225], v203 offset:36864
	ds_read_b128 v[226:229], v203 offset:37888
	ds_read_b128 v[232:235], v203 offset:38912
	ds_read_b128 v[236:239], v203 offset:39936
	global_load_lds_dwordx4 v[240:241], off
	v_lshl_add_u64 v[240:241], s[66:67], 0, v[166:167]
	s_mov_b32 m0, s92
	s_nop 0
	global_load_lds_dwordx4 v[240:241], off
	s_waitcnt vmcnt(8)
	s_waitcnt lgkmcnt(0)
	s_barrier
	s_setprio 1
	s_waitcnt lgkmcnt(0)
	v_mfma_scale_f32_16x16x128_f8f6f4 v[158:161], v[2:9], v[206:213], v[158:161], v204, v204 op_sel_hi:[0,0,0]
	v_mfma_scale_f32_16x16x128_f8f6f4 v[154:157], v[10:17], v[206:213], v[154:157], v204, v204 op_sel_hi:[0,0,0]
	v_mfma_scale_f32_16x16x128_f8f6f4 v[150:153], v[2:9], v[214:221], v[150:153], v204, v204 op_sel_hi:[0,0,0]
	v_mfma_scale_f32_16x16x128_f8f6f4 v[146:149], v[10:17], v[214:221], v[146:149], v204, v204 op_sel_hi:[0,0,0]
	v_mfma_scale_f32_16x16x128_f8f6f4 v[130:133], v[2:9], v[222:229], v[130:133], v204, v204 op_sel_hi:[0,0,0]
	v_mfma_scale_f32_16x16x128_f8f6f4 v[122:125], v[10:17], v[222:229], v[122:125], v204, v204 op_sel_hi:[0,0,0]
	v_mfma_scale_f32_16x16x128_f8f6f4 v[118:121], v[2:9], v[232:239], v[118:121], v204, v204 op_sel_hi:[0,0,0]
	v_mfma_scale_f32_16x16x128_f8f6f4 v[114:117], v[10:17], v[232:239], v[114:117], v204, v204 op_sel_hi:[0,0,0]
	s_setprio 0
	s_setprio 1
	v_mfma_scale_f32_16x16x128_f8f6f4 v[142:145], v[18:25], v[206:213], v[142:145], v204, v204 op_sel_hi:[0,0,0]
	v_mfma_scale_f32_16x16x128_f8f6f4 v[138:141], v[26:33], v[206:213], v[138:141], v204, v204 op_sel_hi:[0,0,0]
	v_mfma_scale_f32_16x16x128_f8f6f4 v[134:137], v[18:25], v[214:221], v[134:137], v204, v204 op_sel_hi:[0,0,0]
	v_mfma_scale_f32_16x16x128_f8f6f4 v[126:129], v[26:33], v[214:221], v[126:129], v204, v204 op_sel_hi:[0,0,0]
	v_mfma_scale_f32_16x16x128_f8f6f4 v[110:113], v[18:25], v[222:229], v[110:113], v204, v204 op_sel_hi:[0,0,0]
	v_mfma_scale_f32_16x16x128_f8f6f4 v[106:109], v[26:33], v[222:229], v[106:109], v204, v204 op_sel_hi:[0,0,0]
	v_mfma_scale_f32_16x16x128_f8f6f4 v[102:105], v[18:25], v[232:239], v[102:105], v204, v204 op_sel_hi:[0,0,0]
	v_mfma_scale_f32_16x16x128_f8f6f4 v[98:101], v[26:33], v[232:239], v[98:101], v204, v204 op_sel_hi:[0,0,0]
	s_setprio 0
	s_barrier
	s_add_i32 s18, s18, s39
	v_lshl_add_u64 v[176:177], v[176:177], 0, s[14:15]
	s_mov_b32 m0, s18
	ds_read_b128 v[206:209], v203 offset:49152
	ds_read_b128 v[210:213], v203 offset:50176
	ds_read_b128 v[214:217], v203 offset:51200
	ds_read_b128 v[218:221], v203 offset:52224
	ds_read_b128 v[222:225], v203 offset:53248
	ds_read_b128 v[226:229], v203 offset:54272
	ds_read_b128 v[232:235], v203 offset:55296
	ds_read_b128 v[236:239], v203 offset:56320
	global_load_lds_dwordx4 v[176:177], off
	s_add_i32 m0, s18, 0x2000
	s_add_u32 s62, s62, 0x40080
	v_lshl_add_u64 v[176:177], v[178:179], 0, s[14:15]
	s_addc_u32 s63, s63, 0
	s_add_i32 s18, s19, s39
	global_load_lds_dwordx4 v[176:177], off
	v_lshl_add_u64 v[176:177], s[62:63], 0, v[164:165]
	s_mov_b32 m0, s18
	s_nop 0
	global_load_lds_dwordx4 v[176:177], off
	v_lshl_add_u64 v[176:177], s[62:63], 0, v[168:169]
	s_add_i32 m0, s18, 0x2000
	s_nop 0
	global_load_lds_dwordx4 v[176:177], off
	v_lshl_add_u64 v[176:177], v[180:181], 0, s[14:15]
	s_mov_b32 m0, s93
	s_nop 0
	global_load_lds_dwordx4 v[176:177], off
	v_lshl_add_u64 v[176:177], v[182:183], 0, s[14:15]
	s_mov_b32 m0, s95
	s_nop 0
	global_load_lds_dwordx4 v[176:177], off
	s_waitcnt vmcnt(8)
	s_waitcnt lgkmcnt(0)
	s_barrier
	s_setprio 1
	s_waitcnt lgkmcnt(0)
	v_mfma_scale_f32_16x16x128_f8f6f4 v[94:97], v[2:9], v[206:213], v[94:97], v204, v204 op_sel_hi:[0,0,0]
	v_mfma_scale_f32_16x16x128_f8f6f4 v[90:93], v[10:17], v[206:213], v[90:93], v204, v204 op_sel_hi:[0,0,0]
	v_mfma_scale_f32_16x16x128_f8f6f4 v[86:89], v[2:9], v[214:221], v[86:89], v204, v204 op_sel_hi:[0,0,0]
	v_mfma_scale_f32_16x16x128_f8f6f4 v[82:85], v[10:17], v[214:221], v[82:85], v204, v204 op_sel_hi:[0,0,0]
	v_mfma_scale_f32_16x16x128_f8f6f4 v[66:69], v[2:9], v[222:229], v[66:69], v204, v204 op_sel_hi:[0,0,0]
	v_mfma_scale_f32_16x16x128_f8f6f4 v[58:61], v[10:17], v[222:229], v[58:61], v204, v204 op_sel_hi:[0,0,0]
	v_mfma_scale_f32_16x16x128_f8f6f4 v[54:57], v[2:9], v[232:239], v[54:57], v204, v204 op_sel_hi:[0,0,0]
	v_mfma_scale_f32_16x16x128_f8f6f4 v[50:53], v[10:17], v[232:239], v[50:53], v204, v204 op_sel_hi:[0,0,0]
	s_setprio 0
	s_setprio 1
	v_mfma_scale_f32_16x16x128_f8f6f4 v[78:81], v[18:25], v[206:213], v[78:81], v204, v204 op_sel_hi:[0,0,0]
	v_mfma_scale_f32_16x16x128_f8f6f4 v[74:77], v[26:33], v[206:213], v[74:77], v204, v204 op_sel_hi:[0,0,0]
	v_mfma_scale_f32_16x16x128_f8f6f4 v[70:73], v[18:25], v[214:221], v[70:73], v204, v204 op_sel_hi:[0,0,0]
	v_mfma_scale_f32_16x16x128_f8f6f4 v[62:65], v[26:33], v[214:221], v[62:65], v204, v204 op_sel_hi:[0,0,0]
	v_mfma_scale_f32_16x16x128_f8f6f4 v[46:49], v[18:25], v[222:229], v[46:49], v204, v204 op_sel_hi:[0,0,0]
	v_mfma_scale_f32_16x16x128_f8f6f4 v[42:45], v[26:33], v[222:229], v[42:45], v204, v204 op_sel_hi:[0,0,0]
	v_mfma_scale_f32_16x16x128_f8f6f4 v[38:41], v[18:25], v[232:239], v[38:41], v204, v204 op_sel_hi:[0,0,0]
	v_mfma_scale_f32_16x16x128_f8f6f4 v[34:37], v[26:33], v[232:239], v[34:37], v204, v204 op_sel_hi:[0,0,0]
	s_setprio 0
	s_add_i32 s71, s71, 2
	s_add_u32 s58, s58, 0x100
	s_addc_u32 s59, s59, 0
	s_add_u32 s69, s69, 0x100
	s_addc_u32 s70, s70, 0
	s_cmp_gt_u32 s71, 13
	s_barrier
	s_cbranch_scc0 .LBB0_285
	s_and_b64 vcc, exec, s[16:17]
	s_cbranch_vccz .LBB0_288
	s_barrier

.LBB0_336:
	ds_read_b128 v[142:145], v1
	ds_read_b128 v[152:155], v1 offset:1024
	ds_read_b128 v[156:159], v1 offset:2048
	ds_read_b128 v[160:163], v1 offset:3072
	ds_read_b128 v[164:167], v149
	ds_read_b128 v[168:171], v149 offset:1024
	ds_read_b128 v[172:175], v149 offset:2048
	ds_read_b128 v[176:179], v149 offset:3072
	s_add_u32 s18, s48, 0xfff80080
	s_addc_u32 s19, s49, -1
	s_cmp_eq_u32 s87, 28
	s_cselect_b32 s55, s17, s19
	s_cselect_b32 s54, s56, s18
	s_cselect_b32 s53, s39, s59
	s_cselect_b32 s52, s57, s58
	v_lshl_add_u64 v[212:213], s[48:49], 0, v[138:139]
	s_add_i32 m0, s47, 0xc000
	ds_read_b128 v[180:183], v150
	ds_read_b128 v[184:187], v150 offset:1024
	ds_read_b128 v[188:191], v150 offset:2048
	ds_read_b128 v[192:195], v150 offset:3072
	ds_read_b128 v[196:199], v150 offset:4096
	ds_read_b128 v[200:203], v150 offset:5120
	ds_read_b128 v[204:207], v150 offset:6144
	ds_read_b128 v[208:211], v150 offset:7168
	global_load_lds_dwordx4 v[212:213], off
	v_lshl_add_u64 v[212:213], s[48:49], 0, v[140:141]
	s_add_i32 m0, s47, 0xe000
	s_nop 0
	global_load_lds_dwordx4 v[212:213], off
	s_waitcnt vmcnt(8)
	s_waitcnt lgkmcnt(0)
	s_barrier
	s_setprio 1
	s_waitcnt lgkmcnt(0)
	v_mfma_f32_16x16x32_bf16 v[126:129], v[142:145], v[180:183], v[126:129]
	v_mfma_f32_16x16x32_bf16 v[122:125], v[156:159], v[180:183], v[122:125]
	v_mfma_f32_16x16x32_bf16 v[114:117], v[142:145], v[188:191], v[114:117]
	v_mfma_f32_16x16x32_bf16 v[106:109], v[156:159], v[188:191], v[106:109]
	v_mfma_f32_16x16x32_bf16 v[98:101], v[142:145], v[196:199], v[98:101]
	v_mfma_f32_16x16x32_bf16 v[90:93], v[156:159], v[196:199], v[90:93]
	v_mfma_f32_16x16x32_bf16 v[82:85], v[142:145], v[204:207], v[82:85]
	v_mfma_f32_16x16x32_bf16 v[74:77], v[156:159], v[204:207], v[74:77]
	v_mfma_f32_16x16x32_bf16 v[126:129], v[152:155], v[184:187], v[126:129]
	v_mfma_f32_16x16x32_bf16 v[122:125], v[160:163], v[184:187], v[122:125]
	v_mfma_f32_16x16x32_bf16 v[114:117], v[152:155], v[192:195], v[114:117]
	v_mfma_f32_16x16x32_bf16 v[106:109], v[160:163], v[192:195], v[106:109]
	v_mfma_f32_16x16x32_bf16 v[98:101], v[152:155], v[200:203], v[98:101]
	v_mfma_f32_16x16x32_bf16 v[90:93], v[160:163], v[200:203], v[90:93]
	v_mfma_f32_16x16x32_bf16 v[82:85], v[152:155], v[208:211], v[82:85]
	v_mfma_f32_16x16x32_bf16 v[74:77], v[160:163], v[208:211], v[74:77]
	s_setprio 0
	s_setprio 1
	v_mfma_f32_16x16x32_bf16 v[118:121], v[164:167], v[180:183], v[118:121]
	v_mfma_f32_16x16x32_bf16 v[110:113], v[172:175], v[180:183], v[110:113]
	v_mfma_f32_16x16x32_bf16 v[102:105], v[164:167], v[188:191], v[102:105]
	v_mfma_f32_16x16x32_bf16 v[94:97], v[172:175], v[188:191], v[94:97]
	v_mfma_f32_16x16x32_bf16 v[86:89], v[164:167], v[196:199], v[86:89]
	v_mfma_f32_16x16x32_bf16 v[78:81], v[172:175], v[196:199], v[78:81]
	v_mfma_f32_16x16x32_bf16 v[70:73], v[164:167], v[204:207], v[70:73]
	v_mfma_f32_16x16x32_bf16 v[66:69], v[172:175], v[204:207], v[66:69]
	v_mfma_f32_16x16x32_bf16 v[118:121], v[168:171], v[184:187], v[118:121]
	v_mfma_f32_16x16x32_bf16 v[110:113], v[176:179], v[184:187], v[110:113]
	v_mfma_f32_16x16x32_bf16 v[102:105], v[168:171], v[192:195], v[102:105]
	v_mfma_f32_16x16x32_bf16 v[94:97], v[176:179], v[192:195], v[94:97]
	v_mfma_f32_16x16x32_bf16 v[86:89], v[168:171], v[200:203], v[86:89]
	v_mfma_f32_16x16x32_bf16 v[78:81], v[176:179], v[200:203], v[78:81]
	v_mfma_f32_16x16x32_bf16 v[70:73], v[168:171], v[208:211], v[70:73]
	v_mfma_f32_16x16x32_bf16 v[66:69], v[176:179], v[208:211], v[66:69]
	s_setprio 0
	s_barrier
	s_add_i32 s18, s71, s30
	v_lshl_add_u64 v[212:213], s[52:53], 0, v[132:133]
	s_mov_b32 m0, s18
	ds_read_b128 v[180:183], v150 offset:16384
	ds_read_b128 v[184:187], v150 offset:17408
	ds_read_b128 v[188:191], v150 offset:18432
	ds_read_b128 v[192:195], v150 offset:19456
	ds_read_b128 v[196:199], v150 offset:20480
	ds_read_b128 v[200:203], v150 offset:21504
	ds_read_b128 v[204:207], v150 offset:22528
	ds_read_b128 v[208:211], v150 offset:23552
	global_load_lds_dwordx4 v[212:213], off
	s_add_i32 m0, s18, 0x2000
	s_add_u32 s90, s52, 0x80000
	v_lshl_add_u64 v[214:215], s[52:53], 0, v[136:137]
	s_addc_u32 s91, s53, 0
	s_add_i32 s18, s84, s30
	global_load_lds_dwordx4 v[214:215], off
	v_lshl_add_u64 v[216:217], s[90:91], 0, v[132:133]
	s_mov_b32 m0, s18
	v_lshl_add_u64 v[218:219], s[54:55], 0, v[134:135]
	global_load_lds_dwordx4 v[216:217], off
	v_lshl_add_u64 v[216:217], s[90:91], 0, v[136:137]
	s_add_i32 m0, s18, 0x2000
	s_nop 0
	global_load_lds_dwordx4 v[216:217], off
	v_lshl_add_u64 v[216:217], s[54:55], 0, v[130:131]
	s_mov_b32 m0, s47
	s_nop 0
	global_load_lds_dwordx4 v[216:217], off
	s_mov_b32 m0, s63
	s_nop 0
	global_load_lds_dwordx4 v[218:219], off
	s_waitcnt vmcnt(8)
	s_waitcnt lgkmcnt(0)
	s_barrier
	s_setprio 1
	s_waitcnt lgkmcnt(0)
	v_mfma_f32_16x16x32_bf16 v[62:65], v[142:145], v[180:183], v[62:65]
	v_mfma_f32_16x16x32_bf16 v[58:61], v[156:159], v[180:183], v[58:61]
	v_mfma_f32_16x16x32_bf16 v[50:53], v[142:145], v[188:191], v[50:53]
	v_mfma_f32_16x16x32_bf16 v[42:45], v[156:159], v[188:191], v[42:45]
	v_mfma_f32_16x16x32_bf16 v[34:37], v[142:145], v[196:199], v[34:37]
	v_mfma_f32_16x16x32_bf16 v[26:29], v[156:159], v[196:199], v[26:29]
	v_mfma_f32_16x16x32_bf16 v[18:21], v[142:145], v[204:207], v[18:21]
	v_mfma_f32_16x16x32_bf16 v[10:13], v[156:159], v[204:207], v[10:13]
	v_mfma_f32_16x16x32_bf16 v[62:65], v[152:155], v[184:187], v[62:65]
	v_mfma_f32_16x16x32_bf16 v[58:61], v[160:163], v[184:187], v[58:61]
	v_mfma_f32_16x16x32_bf16 v[50:53], v[152:155], v[192:195], v[50:53]
	v_mfma_f32_16x16x32_bf16 v[42:45], v[160:163], v[192:195], v[42:45]
	v_mfma_f32_16x16x32_bf16 v[34:37], v[152:155], v[200:203], v[34:37]
	v_mfma_f32_16x16x32_bf16 v[26:29], v[160:163], v[200:203], v[26:29]
	v_mfma_f32_16x16x32_bf16 v[18:21], v[152:155], v[208:211], v[18:21]
	v_mfma_f32_16x16x32_bf16 v[10:13], v[160:163], v[208:211], v[10:13]
	s_setprio 0
	s_setprio 1
	v_mfma_f32_16x16x32_bf16 v[54:57], v[164:167], v[180:183], v[54:57]
	v_mfma_f32_16x16x32_bf16 v[46:49], v[172:175], v[180:183], v[46:49]
	v_mfma_f32_16x16x32_bf16 v[38:41], v[164:167], v[188:191], v[38:41]
	v_mfma_f32_16x16x32_bf16 v[30:33], v[172:175], v[188:191], v[30:33]
	v_mfma_f32_16x16x32_bf16 v[22:25], v[164:167], v[196:199], v[22:25]
	v_mfma_f32_16x16x32_bf16 v[14:17], v[172:175], v[196:199], v[14:17]
	v_mfma_f32_16x16x32_bf16 v[6:9], v[164:167], v[204:207], v[6:9]
	v_mfma_f32_16x16x32_bf16 v[2:5], v[172:175], v[204:207], v[2:5]
	v_mfma_f32_16x16x32_bf16 v[54:57], v[168:171], v[184:187], v[54:57]
	v_mfma_f32_16x16x32_bf16 v[46:49], v[176:179], v[184:187], v[46:49]
	v_mfma_f32_16x16x32_bf16 v[38:41], v[168:171], v[192:195], v[38:41]
	v_mfma_f32_16x16x32_bf16 v[30:33], v[176:179], v[192:195], v[30:33]
	v_mfma_f32_16x16x32_bf16 v[22:25], v[168:171], v[200:203], v[22:25]
	v_mfma_f32_16x16x32_bf16 v[14:17], v[176:179], v[200:203], v[14:17]
	v_mfma_f32_16x16x32_bf16 v[6:9], v[168:171], v[208:211], v[6:9]
	v_mfma_f32_16x16x32_bf16 v[2:5], v[176:179], v[208:211], v[2:5]
	s_setprio 0
	s_barrier
	s_add_i32 s18, 0, 0x18000
	v_add_u32_e32 v151, s18, v147
	s_add_i32 s19, 0, 0x1c000
	ds_read_b128 v[142:145], v151
	ds_read_b128 v[152:155], v151 offset:1024
	ds_read_b128 v[156:159], v151 offset:2048
	ds_read_b128 v[160:163], v151 offset:3072
	v_add_u32_e32 v151, s19, v147
	ds_read_b128 v[164:167], v151
	ds_read_b128 v[168:171], v151 offset:1024
	ds_read_b128 v[172:175], v151 offset:2048
	ds_read_b128 v[176:179], v151 offset:3072
	s_add_u32 s54, s54, 0x80000
	s_addc_u32 s55, s55, 0
	s_mov_b32 m0, s66
	v_lshl_add_u64 v[220:221], s[54:55], 0, v[130:131]
	ds_read_b128 v[180:183], v150 offset:32768
	ds_read_b128 v[184:187], v150 offset:33792
	ds_read_b128 v[188:191], v150 offset:34816
	ds_read_b128 v[192:195], v150 offset:35840
	ds_read_b128 v[196:199], v150 offset:36864
	ds_read_b128 v[200:203], v150 offset:37888
	ds_read_b128 v[204:207], v150 offset:38912
	ds_read_b128 v[208:211], v150 offset:39936
	global_load_lds_dwordx4 v[220:221], off
	v_lshl_add_u64 v[220:221], s[54:55], 0, v[134:135]
	s_mov_b32 m0, s67
	s_nop 0
	global_load_lds_dwordx4 v[220:221], off
	s_waitcnt vmcnt(8)
	s_waitcnt lgkmcnt(0)
	s_barrier
	s_setprio 1
	s_waitcnt lgkmcnt(0)
	v_mfma_f32_16x16x32_bf16 v[126:129], v[142:145], v[180:183], v[126:129]
	v_mfma_f32_16x16x32_bf16 v[122:125], v[156:159], v[180:183], v[122:125]
	v_mfma_f32_16x16x32_bf16 v[114:117], v[142:145], v[188:191], v[114:117]
	v_mfma_f32_16x16x32_bf16 v[106:109], v[156:159], v[188:191], v[106:109]
	v_mfma_f32_16x16x32_bf16 v[98:101], v[142:145], v[196:199], v[98:101]
	v_mfma_f32_16x16x32_bf16 v[90:93], v[156:159], v[196:199], v[90:93]
	v_mfma_f32_16x16x32_bf16 v[82:85], v[142:145], v[204:207], v[82:85]
	v_mfma_f32_16x16x32_bf16 v[74:77], v[156:159], v[204:207], v[74:77]
	v_mfma_f32_16x16x32_bf16 v[126:129], v[152:155], v[184:187], v[126:129]
	v_mfma_f32_16x16x32_bf16 v[122:125], v[160:163], v[184:187], v[122:125]
	v_mfma_f32_16x16x32_bf16 v[114:117], v[152:155], v[192:195], v[114:117]
	v_mfma_f32_16x16x32_bf16 v[106:109], v[160:163], v[192:195], v[106:109]
	v_mfma_f32_16x16x32_bf16 v[98:101], v[152:155], v[200:203], v[98:101]
	v_mfma_f32_16x16x32_bf16 v[90:93], v[160:163], v[200:203], v[90:93]
	v_mfma_f32_16x16x32_bf16 v[82:85], v[152:155], v[208:211], v[82:85]
	v_mfma_f32_16x16x32_bf16 v[74:77], v[160:163], v[208:211], v[74:77]
	s_setprio 0
	s_setprio 1
	v_mfma_f32_16x16x32_bf16 v[118:121], v[164:167], v[180:183], v[118:121]
	v_mfma_f32_16x16x32_bf16 v[110:113], v[172:175], v[180:183], v[110:113]
	v_mfma_f32_16x16x32_bf16 v[102:105], v[164:167], v[188:191], v[102:105]
	v_mfma_f32_16x16x32_bf16 v[94:97], v[172:175], v[188:191], v[94:97]
	v_mfma_f32_16x16x32_bf16 v[86:89], v[164:167], v[196:199], v[86:89]
	v_mfma_f32_16x16x32_bf16 v[78:81], v[172:175], v[196:199], v[78:81]
	v_mfma_f32_16x16x32_bf16 v[70:73], v[164:167], v[204:207], v[70:73]
	v_mfma_f32_16x16x32_bf16 v[66:69], v[172:175], v[204:207], v[66:69]
	v_mfma_f32_16x16x32_bf16 v[118:121], v[168:171], v[184:187], v[118:121]
	v_mfma_f32_16x16x32_bf16 v[110:113], v[176:179], v[184:187], v[110:113]
	v_mfma_f32_16x16x32_bf16 v[102:105], v[168:171], v[192:195], v[102:105]
	v_mfma_f32_16x16x32_bf16 v[94:97], v[176:179], v[192:195], v[94:97]
	v_mfma_f32_16x16x32_bf16 v[86:89], v[168:171], v[200:203], v[86:89]
	v_mfma_f32_16x16x32_bf16 v[78:81], v[176:179], v[200:203], v[78:81]
	v_mfma_f32_16x16x32_bf16 v[70:73], v[168:171], v[208:211], v[70:73]
	v_mfma_f32_16x16x32_bf16 v[66:69], v[176:179], v[208:211], v[66:69]
	s_setprio 0
	s_barrier
	s_add_i32 s18, s18, s30
	v_lshl_add_u64 v[212:213], v[212:213], 0, s[12:13]
	s_mov_b32 m0, s18
	ds_read_b128 v[180:183], v150 offset:49152
	ds_read_b128 v[184:187], v150 offset:50176
	ds_read_b128 v[188:191], v150 offset:51200
	ds_read_b128 v[192:195], v150 offset:52224
	ds_read_b128 v[196:199], v150 offset:53248
	ds_read_b128 v[200:203], v150 offset:54272
	ds_read_b128 v[204:207], v150 offset:55296
	ds_read_b128 v[208:211], v150 offset:56320
	global_load_lds_dwordx4 v[212:213], off
	s_add_i32 m0, s18, 0x2000
	s_add_u32 s52, s52, 0x80080
	v_lshl_add_u64 v[212:213], v[214:215], 0, s[12:13]
	s_addc_u32 s53, s53, 0
	s_add_i32 s18, s19, s30
	global_load_lds_dwordx4 v[212:213], off
	v_lshl_add_u64 v[212:213], s[52:53], 0, v[132:133]
	s_mov_b32 m0, s18
	s_nop 0
	global_load_lds_dwordx4 v[212:213], off
	v_lshl_add_u64 v[212:213], s[52:53], 0, v[136:137]
	s_add_i32 m0, s18, 0x2000
	s_nop 0
	global_load_lds_dwordx4 v[212:213], off
	v_lshl_add_u64 v[212:213], v[216:217], 0, s[12:13]
	s_mov_b32 m0, s68
	s_nop 0
	global_load_lds_dwordx4 v[212:213], off
	v_lshl_add_u64 v[212:213], v[218:219], 0, s[12:13]
	s_mov_b32 m0, s69
	s_nop 0
	global_load_lds_dwordx4 v[212:213], off
	s_waitcnt vmcnt(8)
	s_waitcnt lgkmcnt(0)
	s_barrier
	s_setprio 1
	s_waitcnt lgkmcnt(0)
	v_mfma_f32_16x16x32_bf16 v[62:65], v[142:145], v[180:183], v[62:65]
	v_mfma_f32_16x16x32_bf16 v[58:61], v[156:159], v[180:183], v[58:61]
	v_mfma_f32_16x16x32_bf16 v[50:53], v[142:145], v[188:191], v[50:53]
	v_mfma_f32_16x16x32_bf16 v[42:45], v[156:159], v[188:191], v[42:45]
	v_mfma_f32_16x16x32_bf16 v[34:37], v[142:145], v[196:199], v[34:37]
	v_mfma_f32_16x16x32_bf16 v[26:29], v[156:159], v[196:199], v[26:29]
	v_mfma_f32_16x16x32_bf16 v[18:21], v[142:145], v[204:207], v[18:21]
	v_mfma_f32_16x16x32_bf16 v[10:13], v[156:159], v[204:207], v[10:13]
	v_mfma_f32_16x16x32_bf16 v[62:65], v[152:155], v[184:187], v[62:65]
	v_mfma_f32_16x16x32_bf16 v[58:61], v[160:163], v[184:187], v[58:61]
	v_mfma_f32_16x16x32_bf16 v[50:53], v[152:155], v[192:195], v[50:53]
	v_mfma_f32_16x16x32_bf16 v[42:45], v[160:163], v[192:195], v[42:45]
	v_mfma_f32_16x16x32_bf16 v[34:37], v[152:155], v[200:203], v[34:37]
	v_mfma_f32_16x16x32_bf16 v[26:29], v[160:163], v[200:203], v[26:29]
	v_mfma_f32_16x16x32_bf16 v[18:21], v[152:155], v[208:211], v[18:21]
	v_mfma_f32_16x16x32_bf16 v[10:13], v[160:163], v[208:211], v[10:13]
	s_setprio 0
	s_setprio 1
	v_mfma_f32_16x16x32_bf16 v[54:57], v[164:167], v[180:183], v[54:57]
	v_mfma_f32_16x16x32_bf16 v[46:49], v[172:175], v[180:183], v[46:49]
	v_mfma_f32_16x16x32_bf16 v[38:41], v[164:167], v[188:191], v[38:41]
	v_mfma_f32_16x16x32_bf16 v[30:33], v[172:175], v[188:191], v[30:33]
	v_mfma_f32_16x16x32_bf16 v[22:25], v[164:167], v[196:199], v[22:25]
	v_mfma_f32_16x16x32_bf16 v[14:17], v[172:175], v[196:199], v[14:17]
	v_mfma_f32_16x16x32_bf16 v[6:9], v[164:167], v[204:207], v[6:9]
	v_mfma_f32_16x16x32_bf16 v[2:5], v[172:175], v[204:207], v[2:5]
	v_mfma_f32_16x16x32_bf16 v[54:57], v[168:171], v[184:187], v[54:57]
	v_mfma_f32_16x16x32_bf16 v[46:49], v[176:179], v[184:187], v[46:49]
	v_mfma_f32_16x16x32_bf16 v[38:41], v[168:171], v[192:195], v[38:41]
	v_mfma_f32_16x16x32_bf16 v[30:33], v[176:179], v[192:195], v[30:33]
	v_mfma_f32_16x16x32_bf16 v[22:25], v[168:171], v[200:203], v[22:25]
	v_mfma_f32_16x16x32_bf16 v[14:17], v[176:179], v[200:203], v[14:17]
	v_mfma_f32_16x16x32_bf16 v[6:9], v[168:171], v[208:211], v[6:9]
	v_mfma_f32_16x16x32_bf16 v[2:5], v[176:179], v[208:211], v[2:5]
	s_setprio 0
	s_add_i32 s87, s87, 2
	s_add_u32 s48, s48, 0x100
	s_addc_u32 s49, s49, 0
	s_add_u32 s58, s58, 0x100
	s_addc_u32 s59, s59, 0
	s_cmp_gt_u32 s87, 29
	s_barrier
	s_cbranch_scc0 .LBB0_336
	s_and_b64 vcc, exec, s[14:15]
	s_cbranch_vccz .LBB0_339
	s_barrier

.LBB0_846:
	v_add_u32_e32 v2, s77, v162
	ds_read_b128 v[150:153], v2
	ds_read_b128 v[154:157], v2 offset:1024
	ds_read_b128 v[158:161], v2 offset:2048
	ds_read_b128 v[166:169], v2 offset:3072
	v_add_u32_e32 v2, s78, v162
	ds_read_b128 v[170:173], v2
	ds_read_b128 v[174:177], v2 offset:1024
	ds_read_b128 v[178:181], v2 offset:2048
	ds_read_b128 v[182:185], v2 offset:3072
	s_add_u32 s18, s54, 0xfff80080
	s_addc_u32 s19, s55, -1
	s_cmp_eq_u32 s87, 28
	s_cselect_b32 s63, s34, s19
	s_cselect_b32 s62, s35, s18
	s_cselect_b32 s59, s45, s86
	s_cselect_b32 s58, s47, s57
	v_lshl_add_u64 v[4:5], s[54:55], 0, v[142:143]
	s_add_i32 m0, s71, 0xc000
	ds_read_b128 v[186:189], v164
	ds_read_b128 v[190:193], v164 offset:1024
	ds_read_b128 v[194:197], v164 offset:2048
	ds_read_b128 v[198:201], v164 offset:3072
	ds_read_b128 v[202:205], v164 offset:4096
	ds_read_b128 v[206:209], v164 offset:5120
	ds_read_b128 v[210:213], v164 offset:6144
	ds_read_b128 v[214:217], v164 offset:7168
	global_load_lds_dwordx4 v[4:5], off
	v_lshl_add_u64 v[4:5], s[54:55], 0, v[144:145]
	s_add_i32 m0, s71, 0xe000
	s_nop 0
	global_load_lds_dwordx4 v[4:5], off
	s_waitcnt vmcnt(8)
	s_waitcnt lgkmcnt(0)
	s_barrier
	s_setprio 1
	s_waitcnt lgkmcnt(0)
	v_mfma_f32_16x16x32_bf16 v[130:133], v[150:153], v[186:189], v[130:133]
	v_mfma_f32_16x16x32_bf16 v[126:129], v[158:161], v[186:189], v[126:129]
	v_mfma_f32_16x16x32_bf16 v[122:125], v[150:153], v[194:197], v[122:125]
	v_mfma_f32_16x16x32_bf16 v[118:121], v[158:161], v[194:197], v[118:121]
	v_mfma_f32_16x16x32_bf16 v[114:117], v[150:153], v[202:205], v[114:117]
	v_mfma_f32_16x16x32_bf16 v[110:113], v[158:161], v[202:205], v[110:113]
	v_mfma_f32_16x16x32_bf16 v[106:109], v[150:153], v[210:213], v[106:109]
	v_mfma_f32_16x16x32_bf16 v[102:105], v[158:161], v[210:213], v[102:105]
	v_mfma_f32_16x16x32_bf16 v[130:133], v[154:157], v[190:193], v[130:133]
	v_mfma_f32_16x16x32_bf16 v[126:129], v[166:169], v[190:193], v[126:129]
	v_mfma_f32_16x16x32_bf16 v[122:125], v[154:157], v[198:201], v[122:125]
	v_mfma_f32_16x16x32_bf16 v[118:121], v[166:169], v[198:201], v[118:121]
	v_mfma_f32_16x16x32_bf16 v[114:117], v[154:157], v[206:209], v[114:117]
	v_mfma_f32_16x16x32_bf16 v[110:113], v[166:169], v[206:209], v[110:113]
	v_mfma_f32_16x16x32_bf16 v[106:109], v[154:157], v[214:217], v[106:109]
	v_mfma_f32_16x16x32_bf16 v[102:105], v[166:169], v[214:217], v[102:105]
	s_setprio 0
	s_setprio 1
	v_mfma_f32_16x16x32_bf16 v[98:101], v[170:173], v[186:189], v[98:101]
	v_mfma_f32_16x16x32_bf16 v[94:97], v[178:181], v[186:189], v[94:97]
	v_mfma_f32_16x16x32_bf16 v[90:93], v[170:173], v[194:197], v[90:93]
	v_mfma_f32_16x16x32_bf16 v[86:89], v[178:181], v[194:197], v[86:89]
	v_mfma_f32_16x16x32_bf16 v[82:85], v[170:173], v[202:205], v[82:85]
	v_mfma_f32_16x16x32_bf16 v[78:81], v[178:181], v[202:205], v[78:81]
	v_mfma_f32_16x16x32_bf16 v[74:77], v[170:173], v[210:213], v[74:77]
	v_mfma_f32_16x16x32_bf16 v[70:73], v[178:181], v[210:213], v[70:73]
	v_mfma_f32_16x16x32_bf16 v[98:101], v[174:177], v[190:193], v[98:101]
	v_mfma_f32_16x16x32_bf16 v[94:97], v[182:185], v[190:193], v[94:97]
	v_mfma_f32_16x16x32_bf16 v[90:93], v[174:177], v[198:201], v[90:93]
	v_mfma_f32_16x16x32_bf16 v[86:89], v[182:185], v[198:201], v[86:89]
	v_mfma_f32_16x16x32_bf16 v[82:85], v[174:177], v[206:209], v[82:85]
	v_mfma_f32_16x16x32_bf16 v[78:81], v[182:185], v[206:209], v[78:81]
	v_mfma_f32_16x16x32_bf16 v[74:77], v[174:177], v[214:217], v[74:77]
	v_mfma_f32_16x16x32_bf16 v[70:73], v[182:185], v[214:217], v[70:73]
	s_setprio 0
	s_barrier
	s_add_i32 s18, s77, s70
	v_lshl_add_u64 v[218:219], s[58:59], 0, v[136:137]
	s_mov_b32 m0, s18
	ds_read_b128 v[186:189], v164 offset:16384
	ds_read_b128 v[190:193], v164 offset:17408
	ds_read_b128 v[194:197], v164 offset:18432
	ds_read_b128 v[198:201], v164 offset:19456
	ds_read_b128 v[202:205], v164 offset:20480
	ds_read_b128 v[206:209], v164 offset:21504
	ds_read_b128 v[210:213], v164 offset:22528
	ds_read_b128 v[214:217], v164 offset:23552
	global_load_lds_dwordx4 v[218:219], off
	s_add_i32 m0, s18, 0x2000
	s_add_u32 s90, s58, 0x80000
	v_lshl_add_u64 v[220:221], s[58:59], 0, v[140:141]
	s_addc_u32 s91, s59, 0
	s_add_i32 s18, s78, s70
	global_load_lds_dwordx4 v[220:221], off
	v_lshl_add_u64 v[4:5], s[90:91], 0, v[136:137]
	s_mov_b32 m0, s18
	v_lshl_add_u64 v[222:223], s[62:63], 0, v[134:135]
	global_load_lds_dwordx4 v[4:5], off
	v_lshl_add_u64 v[4:5], s[90:91], 0, v[140:141]
	s_add_i32 m0, s18, 0x2000
	v_lshl_add_u64 v[224:225], s[62:63], 0, v[138:139]
	global_load_lds_dwordx4 v[4:5], off
	s_mov_b32 m0, s71
	s_nop 0
	global_load_lds_dwordx4 v[222:223], off
	s_mov_b32 m0, s72
	s_nop 0
	global_load_lds_dwordx4 v[224:225], off
	s_waitcnt vmcnt(8)
	s_waitcnt lgkmcnt(0)
	s_barrier
	s_setprio 1
	s_waitcnt lgkmcnt(0)
	v_mfma_f32_16x16x32_bf16 v[66:69], v[150:153], v[186:189], v[66:69]
	v_mfma_f32_16x16x32_bf16 v[62:65], v[158:161], v[186:189], v[62:65]
	v_mfma_f32_16x16x32_bf16 v[58:61], v[150:153], v[194:197], v[58:61]
	v_mfma_f32_16x16x32_bf16 v[54:57], v[158:161], v[194:197], v[54:57]
	v_mfma_f32_16x16x32_bf16 v[50:53], v[150:153], v[202:205], v[50:53]
	v_mfma_f32_16x16x32_bf16 v[46:49], v[158:161], v[202:205], v[46:49]
	v_mfma_f32_16x16x32_bf16 v[42:45], v[150:153], v[210:213], v[42:45]
	v_mfma_f32_16x16x32_bf16 v[38:41], v[158:161], v[210:213], v[38:41]
	v_mfma_f32_16x16x32_bf16 v[66:69], v[154:157], v[190:193], v[66:69]
	v_mfma_f32_16x16x32_bf16 v[62:65], v[166:169], v[190:193], v[62:65]
	v_mfma_f32_16x16x32_bf16 v[58:61], v[154:157], v[198:201], v[58:61]
	v_mfma_f32_16x16x32_bf16 v[54:57], v[166:169], v[198:201], v[54:57]
	v_mfma_f32_16x16x32_bf16 v[50:53], v[154:157], v[206:209], v[50:53]
	v_mfma_f32_16x16x32_bf16 v[46:49], v[166:169], v[206:209], v[46:49]
	v_mfma_f32_16x16x32_bf16 v[42:45], v[154:157], v[214:217], v[42:45]
	v_mfma_f32_16x16x32_bf16 v[38:41], v[166:169], v[214:217], v[38:41]
	s_setprio 0
	s_setprio 1
	v_mfma_f32_16x16x32_bf16 v[34:37], v[170:173], v[186:189], v[34:37]
	v_mfma_f32_16x16x32_bf16 v[30:33], v[178:181], v[186:189], v[30:33]
	v_mfma_f32_16x16x32_bf16 v[26:29], v[170:173], v[194:197], v[26:29]
	v_mfma_f32_16x16x32_bf16 v[22:25], v[178:181], v[194:197], v[22:25]
	v_mfma_f32_16x16x32_bf16 v[18:21], v[170:173], v[202:205], v[18:21]
	v_mfma_f32_16x16x32_bf16 v[14:17], v[178:181], v[202:205], v[14:17]
	v_mfma_f32_16x16x32_bf16 v[10:13], v[170:173], v[210:213], v[10:13]
	v_mfma_f32_16x16x32_bf16 v[4:7], v[178:181], v[210:213], v[6:9]
	v_mfma_f32_16x16x32_bf16 v[34:37], v[174:177], v[190:193], v[34:37]
	v_mfma_f32_16x16x32_bf16 v[30:33], v[182:185], v[190:193], v[30:33]
	v_mfma_f32_16x16x32_bf16 v[26:29], v[174:177], v[198:201], v[26:29]
	v_mfma_f32_16x16x32_bf16 v[22:25], v[182:185], v[198:201], v[22:25]
	v_mfma_f32_16x16x32_bf16 v[18:21], v[174:177], v[206:209], v[18:21]
	v_mfma_f32_16x16x32_bf16 v[14:17], v[182:185], v[206:209], v[14:17]
	v_mfma_f32_16x16x32_bf16 v[10:13], v[174:177], v[214:217], v[10:13]
	v_mfma_f32_16x16x32_bf16 v[4:7], v[182:185], v[214:217], v[4:7]
	s_setprio 0
	s_barrier
	s_add_i32 s18, 0, 0x18000
	v_add_u32_e32 v2, s18, v162
	s_add_i32 s19, 0, 0x1c000
	ds_read_b128 v[150:153], v2
	ds_read_b128 v[154:157], v2 offset:1024
	ds_read_b128 v[158:161], v2 offset:2048
	ds_read_b128 v[166:169], v2 offset:3072
	v_add_u32_e32 v2, s19, v162
	ds_read_b128 v[170:173], v2
	ds_read_b128 v[174:177], v2 offset:1024
	ds_read_b128 v[178:181], v2 offset:2048
	ds_read_b128 v[182:185], v2 offset:3072
	s_add_u32 s62, s62, 0x80000
	s_addc_u32 s63, s63, 0
	s_mov_b32 m0, s73
	v_lshl_add_u64 v[8:9], s[62:63], 0, v[134:135]
	ds_read_b128 v[186:189], v164 offset:32768
	ds_read_b128 v[190:193], v164 offset:33792
	ds_read_b128 v[194:197], v164 offset:34816
	ds_read_b128 v[198:201], v164 offset:35840
	ds_read_b128 v[202:205], v164 offset:36864
	ds_read_b128 v[206:209], v164 offset:37888
	ds_read_b128 v[210:213], v164 offset:38912
	ds_read_b128 v[214:217], v164 offset:39936
	global_load_lds_dwordx4 v[8:9], off
	v_lshl_add_u64 v[8:9], s[62:63], 0, v[138:139]
	s_mov_b32 m0, s74
	s_nop 0
	global_load_lds_dwordx4 v[8:9], off
	s_waitcnt vmcnt(8)
	s_waitcnt lgkmcnt(0)
	s_barrier
	s_setprio 1
	s_waitcnt lgkmcnt(0)
	v_mfma_f32_16x16x32_bf16 v[130:133], v[150:153], v[186:189], v[130:133]
	v_mfma_f32_16x16x32_bf16 v[126:129], v[158:161], v[186:189], v[126:129]
	v_mfma_f32_16x16x32_bf16 v[122:125], v[150:153], v[194:197], v[122:125]
	v_mfma_f32_16x16x32_bf16 v[118:121], v[158:161], v[194:197], v[118:121]
	v_mfma_f32_16x16x32_bf16 v[114:117], v[150:153], v[202:205], v[114:117]
	v_mfma_f32_16x16x32_bf16 v[110:113], v[158:161], v[202:205], v[110:113]
	v_mfma_f32_16x16x32_bf16 v[106:109], v[150:153], v[210:213], v[106:109]
	v_mfma_f32_16x16x32_bf16 v[102:105], v[158:161], v[210:213], v[102:105]
	v_mfma_f32_16x16x32_bf16 v[130:133], v[154:157], v[190:193], v[130:133]
	v_mfma_f32_16x16x32_bf16 v[126:129], v[166:169], v[190:193], v[126:129]
	v_mfma_f32_16x16x32_bf16 v[122:125], v[154:157], v[198:201], v[122:125]
	v_mfma_f32_16x16x32_bf16 v[118:121], v[166:169], v[198:201], v[118:121]
	v_mfma_f32_16x16x32_bf16 v[114:117], v[154:157], v[206:209], v[114:117]
	v_mfma_f32_16x16x32_bf16 v[110:113], v[166:169], v[206:209], v[110:113]
	v_mfma_f32_16x16x32_bf16 v[106:109], v[154:157], v[214:217], v[106:109]
	v_mfma_f32_16x16x32_bf16 v[102:105], v[166:169], v[214:217], v[102:105]
	s_setprio 0
	s_setprio 1
	v_mfma_f32_16x16x32_bf16 v[98:101], v[170:173], v[186:189], v[98:101]
	v_mfma_f32_16x16x32_bf16 v[94:97], v[178:181], v[186:189], v[94:97]
	v_mfma_f32_16x16x32_bf16 v[90:93], v[170:173], v[194:197], v[90:93]
	v_mfma_f32_16x16x32_bf16 v[86:89], v[178:181], v[194:197], v[86:89]
	v_mfma_f32_16x16x32_bf16 v[82:85], v[170:173], v[202:205], v[82:85]
	v_mfma_f32_16x16x32_bf16 v[78:81], v[178:181], v[202:205], v[78:81]
	v_mfma_f32_16x16x32_bf16 v[74:77], v[170:173], v[210:213], v[74:77]
	v_mfma_f32_16x16x32_bf16 v[70:73], v[178:181], v[210:213], v[70:73]
	v_mfma_f32_16x16x32_bf16 v[98:101], v[174:177], v[190:193], v[98:101]
	v_mfma_f32_16x16x32_bf16 v[94:97], v[182:185], v[190:193], v[94:97]
	v_mfma_f32_16x16x32_bf16 v[90:93], v[174:177], v[198:201], v[90:93]
	v_mfma_f32_16x16x32_bf16 v[86:89], v[182:185], v[198:201], v[86:89]
	v_mfma_f32_16x16x32_bf16 v[82:85], v[174:177], v[206:209], v[82:85]
	v_mfma_f32_16x16x32_bf16 v[78:81], v[182:185], v[206:209], v[78:81]
	v_mfma_f32_16x16x32_bf16 v[74:77], v[174:177], v[214:217], v[74:77]
	v_mfma_f32_16x16x32_bf16 v[70:73], v[182:185], v[214:217], v[70:73]
	s_setprio 0
	s_barrier
	s_add_i32 s18, s18, s70
	v_lshl_add_u64 v[8:9], v[218:219], 0, s[14:15]
	s_mov_b32 m0, s18
	ds_read_b128 v[186:189], v164 offset:49152
	ds_read_b128 v[190:193], v164 offset:50176
	ds_read_b128 v[194:197], v164 offset:51200
	ds_read_b128 v[198:201], v164 offset:52224
	ds_read_b128 v[202:205], v164 offset:53248
	ds_read_b128 v[206:209], v164 offset:54272
	ds_read_b128 v[210:213], v164 offset:55296
	ds_read_b128 v[214:217], v164 offset:56320
	global_load_lds_dwordx4 v[8:9], off
	s_add_i32 m0, s18, 0x2000
	s_add_u32 s58, s58, 0x80080
	v_lshl_add_u64 v[8:9], v[220:221], 0, s[14:15]
	s_addc_u32 s59, s59, 0
	s_add_i32 s18, s19, s70
	global_load_lds_dwordx4 v[8:9], off
	v_lshl_add_u64 v[8:9], s[58:59], 0, v[136:137]
	s_mov_b32 m0, s18
	s_nop 0
	global_load_lds_dwordx4 v[8:9], off
	v_lshl_add_u64 v[8:9], s[58:59], 0, v[140:141]
	s_add_i32 m0, s18, 0x2000
	s_nop 0
	global_load_lds_dwordx4 v[8:9], off
	v_lshl_add_u64 v[8:9], v[222:223], 0, s[14:15]
	s_mov_b32 m0, s75
	s_nop 0
	global_load_lds_dwordx4 v[8:9], off
	v_lshl_add_u64 v[8:9], v[224:225], 0, s[14:15]
	s_mov_b32 m0, s76
	s_nop 0
	global_load_lds_dwordx4 v[8:9], off
	s_waitcnt vmcnt(8)
	s_waitcnt lgkmcnt(0)
	s_barrier
	s_setprio 1
	s_waitcnt lgkmcnt(0)
	v_mfma_f32_16x16x32_bf16 v[66:69], v[150:153], v[186:189], v[66:69]
	v_mfma_f32_16x16x32_bf16 v[62:65], v[158:161], v[186:189], v[62:65]
	v_mfma_f32_16x16x32_bf16 v[58:61], v[150:153], v[194:197], v[58:61]
	v_mfma_f32_16x16x32_bf16 v[54:57], v[158:161], v[194:197], v[54:57]
	v_mfma_f32_16x16x32_bf16 v[50:53], v[150:153], v[202:205], v[50:53]
	v_mfma_f32_16x16x32_bf16 v[46:49], v[158:161], v[202:205], v[46:49]
	v_mfma_f32_16x16x32_bf16 v[42:45], v[150:153], v[210:213], v[42:45]
	v_mfma_f32_16x16x32_bf16 v[38:41], v[158:161], v[210:213], v[38:41]
	v_mfma_f32_16x16x32_bf16 v[66:69], v[154:157], v[190:193], v[66:69]
	v_mfma_f32_16x16x32_bf16 v[62:65], v[166:169], v[190:193], v[62:65]
	v_mfma_f32_16x16x32_bf16 v[58:61], v[154:157], v[198:201], v[58:61]
	v_mfma_f32_16x16x32_bf16 v[54:57], v[166:169], v[198:201], v[54:57]
	v_mfma_f32_16x16x32_bf16 v[50:53], v[154:157], v[206:209], v[50:53]
	v_mfma_f32_16x16x32_bf16 v[46:49], v[166:169], v[206:209], v[46:49]
	v_mfma_f32_16x16x32_bf16 v[42:45], v[154:157], v[214:217], v[42:45]
	v_mfma_f32_16x16x32_bf16 v[38:41], v[166:169], v[214:217], v[38:41]
	s_setprio 0
	s_setprio 1
	v_mfma_f32_16x16x32_bf16 v[34:37], v[170:173], v[186:189], v[34:37]
	v_mfma_f32_16x16x32_bf16 v[30:33], v[178:181], v[186:189], v[30:33]
	v_mfma_f32_16x16x32_bf16 v[26:29], v[170:173], v[194:197], v[26:29]
	v_mfma_f32_16x16x32_bf16 v[22:25], v[178:181], v[194:197], v[22:25]
	v_mfma_f32_16x16x32_bf16 v[18:21], v[170:173], v[202:205], v[18:21]
	v_mfma_f32_16x16x32_bf16 v[14:17], v[178:181], v[202:205], v[14:17]
	v_mfma_f32_16x16x32_bf16 v[8:11], v[170:173], v[210:213], v[10:13]
	v_mfma_f32_16x16x32_bf16 v[4:7], v[178:181], v[210:213], v[4:7]
	v_mfma_f32_16x16x32_bf16 v[34:37], v[174:177], v[190:193], v[34:37]
	v_mfma_f32_16x16x32_bf16 v[30:33], v[182:185], v[190:193], v[30:33]
	v_mfma_f32_16x16x32_bf16 v[26:29], v[174:177], v[198:201], v[26:29]
	v_mfma_f32_16x16x32_bf16 v[22:25], v[182:185], v[198:201], v[22:25]
	v_mfma_f32_16x16x32_bf16 v[18:21], v[174:177], v[206:209], v[18:21]
	v_mfma_f32_16x16x32_bf16 v[14:17], v[182:185], v[206:209], v[14:17]
	v_mfma_f32_16x16x32_bf16 v[10:13], v[174:177], v[214:217], v[8:11]
	v_mfma_f32_16x16x32_bf16 v[6:9], v[182:185], v[214:217], v[4:7]
	s_setprio 0
	s_add_i32 s87, s87, 2
	s_add_u32 s54, s54, 0x100
	s_addc_u32 s55, s55, 0
	s_add_u32 s57, s57, 0x100
	s_addc_u32 s86, s86, 0
	s_cmp_gt_u32 s87, 29
	s_barrier
	s_cbranch_scc0 .LBB0_846
	s_and_b64 vcc, exec, s[16:17]
	s_cbranch_vccz .LBB0_849
	s_barrier

.LBB0_927:
	ds_read_b128 v[130:133], v166
	ds_read_b128 v[134:137], v166 offset:1024
	ds_read_b128 v[138:141], v166 offset:2048
	ds_read_b128 v[142:145], v166 offset:3072
	ds_read_b128 v[170:173], v167
	ds_read_b128 v[174:177], v167 offset:1024
	ds_read_b128 v[178:181], v167 offset:2048
	ds_read_b128 v[182:185], v167 offset:3072
	s_add_u32 s18, s56, 0xfff80080
	s_addc_u32 s19, s57, -1
	s_cmp_eq_u32 s86, 28
	s_cselect_b32 s63, s47, s19
	s_cselect_b32 s62, s82, s18
	s_cselect_b32 s59, s45, s85
	s_cselect_b32 s58, s83, s84
	v_lshl_add_u64 v[162:163], s[56:57], 0, v[154:155]
	s_add_i32 m0, s55, 0xc000
	ds_read_b128 v[186:189], v168
	ds_read_b128 v[190:193], v168 offset:1024
	ds_read_b128 v[194:197], v168 offset:2048
	ds_read_b128 v[198:201], v168 offset:3072
	ds_read_b128 v[202:205], v168 offset:4096
	ds_read_b128 v[206:209], v168 offset:5120
	ds_read_b128 v[210:213], v168 offset:6144
	ds_read_b128 v[214:217], v168 offset:7168
	global_load_lds_dwordx4 v[162:163], off
	v_lshl_add_u64 v[162:163], s[56:57], 0, v[156:157]
	s_add_i32 m0, s55, 0xe000
	s_nop 0
	global_load_lds_dwordx4 v[162:163], off
	s_waitcnt vmcnt(8)
	s_waitcnt lgkmcnt(0)
	s_barrier
	s_setprio 1
	s_waitcnt lgkmcnt(0)
	v_mfma_f32_16x16x32_bf16 v[122:125], v[130:133], v[186:189], v[122:125]
	v_mfma_f32_16x16x32_bf16 v[126:129], v[138:141], v[186:189], v[126:129]
	v_mfma_f32_16x16x32_bf16 v[114:117], v[130:133], v[194:197], v[114:117]
	v_mfma_f32_16x16x32_bf16 v[118:121], v[138:141], v[194:197], v[118:121]
	v_mfma_f32_16x16x32_bf16 v[102:105], v[130:133], v[202:205], v[102:105]
	v_mfma_f32_16x16x32_bf16 v[110:113], v[138:141], v[202:205], v[110:113]
	v_mfma_f32_16x16x32_bf16 v[94:97], v[130:133], v[210:213], v[94:97]
	v_mfma_f32_16x16x32_bf16 v[74:77], v[138:141], v[210:213], v[74:77]
	v_mfma_f32_16x16x32_bf16 v[122:125], v[134:137], v[190:193], v[122:125]
	v_mfma_f32_16x16x32_bf16 v[126:129], v[142:145], v[190:193], v[126:129]
	v_mfma_f32_16x16x32_bf16 v[114:117], v[134:137], v[198:201], v[114:117]
	v_mfma_f32_16x16x32_bf16 v[118:121], v[142:145], v[198:201], v[118:121]
	v_mfma_f32_16x16x32_bf16 v[102:105], v[134:137], v[206:209], v[102:105]
	v_mfma_f32_16x16x32_bf16 v[110:113], v[142:145], v[206:209], v[110:113]
	v_mfma_f32_16x16x32_bf16 v[94:97], v[134:137], v[214:217], v[94:97]
	v_mfma_f32_16x16x32_bf16 v[74:77], v[142:145], v[214:217], v[74:77]
	s_setprio 0
	s_setprio 1
	v_mfma_f32_16x16x32_bf16 v[106:109], v[170:173], v[186:189], v[106:109]
	v_mfma_f32_16x16x32_bf16 v[90:93], v[178:181], v[186:189], v[90:93]
	v_mfma_f32_16x16x32_bf16 v[98:101], v[170:173], v[194:197], v[98:101]
	v_mfma_f32_16x16x32_bf16 v[82:85], v[178:181], v[194:197], v[82:85]
	v_mfma_f32_16x16x32_bf16 v[86:89], v[170:173], v[202:205], v[86:89]
	v_mfma_f32_16x16x32_bf16 v[78:81], v[178:181], v[202:205], v[78:81]
	v_mfma_f32_16x16x32_bf16 v[70:73], v[170:173], v[210:213], v[70:73]
	v_mfma_f32_16x16x32_bf16 v[66:69], v[178:181], v[210:213], v[66:69]
	v_mfma_f32_16x16x32_bf16 v[106:109], v[174:177], v[190:193], v[106:109]
	v_mfma_f32_16x16x32_bf16 v[90:93], v[182:185], v[190:193], v[90:93]
	v_mfma_f32_16x16x32_bf16 v[98:101], v[174:177], v[198:201], v[98:101]
	v_mfma_f32_16x16x32_bf16 v[82:85], v[182:185], v[198:201], v[82:85]
	v_mfma_f32_16x16x32_bf16 v[86:89], v[174:177], v[206:209], v[86:89]
	v_mfma_f32_16x16x32_bf16 v[78:81], v[182:185], v[206:209], v[78:81]
	v_mfma_f32_16x16x32_bf16 v[70:73], v[174:177], v[214:217], v[70:73]
	v_mfma_f32_16x16x32_bf16 v[66:69], v[182:185], v[214:217], v[66:69]
	s_setprio 0
	s_barrier
	s_add_i32 s18, s74, s66
	v_lshl_add_u64 v[162:163], s[58:59], 0, v[148:149]
	s_mov_b32 m0, s18
	ds_read_b128 v[186:189], v168 offset:16384
	ds_read_b128 v[190:193], v168 offset:17408
	ds_read_b128 v[194:197], v168 offset:18432
	ds_read_b128 v[198:201], v168 offset:19456
	ds_read_b128 v[202:205], v168 offset:20480
	ds_read_b128 v[206:209], v168 offset:21504
	ds_read_b128 v[210:213], v168 offset:22528
	ds_read_b128 v[214:217], v168 offset:23552
	global_load_lds_dwordx4 v[162:163], off
	s_add_i32 m0, s18, 0x2000
	s_add_u32 s90, s58, 0x80000
	v_lshl_add_u64 v[218:219], s[58:59], 0, v[152:153]
	s_addc_u32 s91, s59, 0
	s_add_i32 s18, s75, s66
	global_load_lds_dwordx4 v[218:219], off
	v_lshl_add_u64 v[220:221], s[90:91], 0, v[148:149]
	s_mov_b32 m0, s18
	v_lshl_add_u64 v[222:223], s[62:63], 0, v[150:151]
	global_load_lds_dwordx4 v[220:221], off
	v_lshl_add_u64 v[220:221], s[90:91], 0, v[152:153]
	s_add_i32 m0, s18, 0x2000
	s_nop 0
	global_load_lds_dwordx4 v[220:221], off
	v_lshl_add_u64 v[220:221], s[62:63], 0, v[146:147]
	s_mov_b32 m0, s55
	s_nop 0
	global_load_lds_dwordx4 v[220:221], off
	s_mov_b32 m0, s67
	s_nop 0
	global_load_lds_dwordx4 v[222:223], off
	s_waitcnt vmcnt(8)
	s_waitcnt lgkmcnt(0)
	s_barrier
	s_setprio 1
	s_waitcnt lgkmcnt(0)
	v_mfma_f32_16x16x32_bf16 v[62:65], v[130:133], v[186:189], v[62:65]
	v_mfma_f32_16x16x32_bf16 v[58:61], v[138:141], v[186:189], v[58:61]
	v_mfma_f32_16x16x32_bf16 v[50:53], v[130:133], v[194:197], v[50:53]
	v_mfma_f32_16x16x32_bf16 v[42:45], v[138:141], v[194:197], v[42:45]
	v_mfma_f32_16x16x32_bf16 v[34:37], v[130:133], v[202:205], v[34:37]
	v_mfma_f32_16x16x32_bf16 v[26:29], v[138:141], v[202:205], v[26:29]
	v_mfma_f32_16x16x32_bf16 v[18:21], v[130:133], v[210:213], v[18:21]
	v_mfma_f32_16x16x32_bf16 v[10:13], v[138:141], v[210:213], v[10:13]
	v_mfma_f32_16x16x32_bf16 v[62:65], v[134:137], v[190:193], v[62:65]
	v_mfma_f32_16x16x32_bf16 v[58:61], v[142:145], v[190:193], v[58:61]
	v_mfma_f32_16x16x32_bf16 v[50:53], v[134:137], v[198:201], v[50:53]
	v_mfma_f32_16x16x32_bf16 v[42:45], v[142:145], v[198:201], v[42:45]
	v_mfma_f32_16x16x32_bf16 v[34:37], v[134:137], v[206:209], v[34:37]
	v_mfma_f32_16x16x32_bf16 v[26:29], v[142:145], v[206:209], v[26:29]
	v_mfma_f32_16x16x32_bf16 v[18:21], v[134:137], v[214:217], v[18:21]
	v_mfma_f32_16x16x32_bf16 v[10:13], v[142:145], v[214:217], v[10:13]
	s_setprio 0
	s_setprio 1
	v_mfma_f32_16x16x32_bf16 v[54:57], v[170:173], v[186:189], v[54:57]
	v_mfma_f32_16x16x32_bf16 v[46:49], v[178:181], v[186:189], v[46:49]
	v_mfma_f32_16x16x32_bf16 v[38:41], v[170:173], v[194:197], v[38:41]
	v_mfma_f32_16x16x32_bf16 v[30:33], v[178:181], v[194:197], v[30:33]
	v_mfma_f32_16x16x32_bf16 v[22:25], v[170:173], v[202:205], v[22:25]
	v_mfma_f32_16x16x32_bf16 v[14:17], v[178:181], v[202:205], v[14:17]
	v_mfma_f32_16x16x32_bf16 v[6:9], v[170:173], v[210:213], v[6:9]
	v_mfma_f32_16x16x32_bf16 v[2:5], v[178:181], v[210:213], v[2:5]
	v_mfma_f32_16x16x32_bf16 v[54:57], v[174:177], v[190:193], v[54:57]
	v_mfma_f32_16x16x32_bf16 v[46:49], v[182:185], v[190:193], v[46:49]
	v_mfma_f32_16x16x32_bf16 v[38:41], v[174:177], v[198:201], v[38:41]
	v_mfma_f32_16x16x32_bf16 v[30:33], v[182:185], v[198:201], v[30:33]
	v_mfma_f32_16x16x32_bf16 v[22:25], v[174:177], v[206:209], v[22:25]
	v_mfma_f32_16x16x32_bf16 v[14:17], v[182:185], v[206:209], v[14:17]
	v_mfma_f32_16x16x32_bf16 v[6:9], v[174:177], v[214:217], v[6:9]
	v_mfma_f32_16x16x32_bf16 v[2:5], v[182:185], v[214:217], v[2:5]
	s_setprio 0
	s_barrier
	s_add_i32 s18, 0, 0x18000
	s_add_i32 s19, 0, 0x1c000
	v_add_u32_e32 v142, s18, v164
	v_add_u32_e32 v169, s19, v164
	ds_read_b128 v[130:133], v142
	ds_read_b128 v[134:137], v142 offset:1024
	ds_read_b128 v[138:141], v142 offset:2048
	ds_read_b128 v[142:145], v142 offset:3072
	ds_read_b128 v[170:173], v169
	ds_read_b128 v[174:177], v169 offset:1024
	ds_read_b128 v[178:181], v169 offset:2048
	ds_read_b128 v[182:185], v169 offset:3072
	s_add_u32 s62, s62, 0x80000
	s_addc_u32 s63, s63, 0
	s_mov_b32 m0, s68
	v_lshl_add_u64 v[224:225], s[62:63], 0, v[146:147]
	ds_read_b128 v[186:189], v168 offset:32768
	ds_read_b128 v[190:193], v168 offset:33792
	ds_read_b128 v[194:197], v168 offset:34816
	ds_read_b128 v[198:201], v168 offset:35840
	ds_read_b128 v[202:205], v168 offset:36864
	ds_read_b128 v[206:209], v168 offset:37888
	ds_read_b128 v[210:213], v168 offset:38912
	ds_read_b128 v[214:217], v168 offset:39936
	global_load_lds_dwordx4 v[224:225], off
	v_lshl_add_u64 v[224:225], s[62:63], 0, v[150:151]
	s_mov_b32 m0, s69
	s_nop 0
	global_load_lds_dwordx4 v[224:225], off
	s_waitcnt vmcnt(8)
	s_waitcnt lgkmcnt(0)
	s_barrier
	s_setprio 1
	s_waitcnt lgkmcnt(0)
	v_mfma_f32_16x16x32_bf16 v[122:125], v[130:133], v[186:189], v[122:125]
	v_mfma_f32_16x16x32_bf16 v[126:129], v[138:141], v[186:189], v[126:129]
	v_mfma_f32_16x16x32_bf16 v[114:117], v[130:133], v[194:197], v[114:117]
	v_mfma_f32_16x16x32_bf16 v[118:121], v[138:141], v[194:197], v[118:121]
	v_mfma_f32_16x16x32_bf16 v[102:105], v[130:133], v[202:205], v[102:105]
	v_mfma_f32_16x16x32_bf16 v[110:113], v[138:141], v[202:205], v[110:113]
	v_mfma_f32_16x16x32_bf16 v[94:97], v[130:133], v[210:213], v[94:97]
	v_mfma_f32_16x16x32_bf16 v[74:77], v[138:141], v[210:213], v[74:77]
	v_mfma_f32_16x16x32_bf16 v[122:125], v[134:137], v[190:193], v[122:125]
	v_mfma_f32_16x16x32_bf16 v[126:129], v[142:145], v[190:193], v[126:129]
	v_mfma_f32_16x16x32_bf16 v[114:117], v[134:137], v[198:201], v[114:117]
	v_mfma_f32_16x16x32_bf16 v[118:121], v[142:145], v[198:201], v[118:121]
	v_mfma_f32_16x16x32_bf16 v[102:105], v[134:137], v[206:209], v[102:105]
	v_mfma_f32_16x16x32_bf16 v[110:113], v[142:145], v[206:209], v[110:113]
	v_mfma_f32_16x16x32_bf16 v[94:97], v[134:137], v[214:217], v[94:97]
	v_mfma_f32_16x16x32_bf16 v[74:77], v[142:145], v[214:217], v[74:77]
	s_setprio 0
	s_setprio 1
	v_mfma_f32_16x16x32_bf16 v[106:109], v[170:173], v[186:189], v[106:109]
	v_mfma_f32_16x16x32_bf16 v[90:93], v[178:181], v[186:189], v[90:93]
	v_mfma_f32_16x16x32_bf16 v[98:101], v[170:173], v[194:197], v[98:101]
	v_mfma_f32_16x16x32_bf16 v[82:85], v[178:181], v[194:197], v[82:85]
	v_mfma_f32_16x16x32_bf16 v[86:89], v[170:173], v[202:205], v[86:89]
	v_mfma_f32_16x16x32_bf16 v[78:81], v[178:181], v[202:205], v[78:81]
	v_mfma_f32_16x16x32_bf16 v[70:73], v[170:173], v[210:213], v[70:73]
	v_mfma_f32_16x16x32_bf16 v[66:69], v[178:181], v[210:213], v[66:69]
	v_mfma_f32_16x16x32_bf16 v[106:109], v[174:177], v[190:193], v[106:109]
	v_mfma_f32_16x16x32_bf16 v[90:93], v[182:185], v[190:193], v[90:93]
	v_mfma_f32_16x16x32_bf16 v[98:101], v[174:177], v[198:201], v[98:101]
	v_mfma_f32_16x16x32_bf16 v[82:85], v[182:185], v[198:201], v[82:85]
	v_mfma_f32_16x16x32_bf16 v[86:89], v[174:177], v[206:209], v[86:89]
	v_mfma_f32_16x16x32_bf16 v[78:81], v[182:185], v[206:209], v[78:81]
	v_mfma_f32_16x16x32_bf16 v[70:73], v[174:177], v[214:217], v[70:73]
	v_mfma_f32_16x16x32_bf16 v[66:69], v[182:185], v[214:217], v[66:69]
	s_setprio 0
	s_barrier
	s_add_i32 s18, s18, s66
	v_lshl_add_u64 v[162:163], v[162:163], 0, s[12:13]
	s_mov_b32 m0, s18
	ds_read_b128 v[186:189], v168 offset:49152
	ds_read_b128 v[190:193], v168 offset:50176
	ds_read_b128 v[194:197], v168 offset:51200
	ds_read_b128 v[198:201], v168 offset:52224
	ds_read_b128 v[202:205], v168 offset:53248
	ds_read_b128 v[206:209], v168 offset:54272
	ds_read_b128 v[210:213], v168 offset:55296
	ds_read_b128 v[214:217], v168 offset:56320
	global_load_lds_dwordx4 v[162:163], off
	s_add_i32 m0, s18, 0x2000
	s_add_u32 s58, s58, 0x80080
	v_lshl_add_u64 v[162:163], v[218:219], 0, s[12:13]
	s_addc_u32 s59, s59, 0
	s_add_i32 s18, s19, s66
	global_load_lds_dwordx4 v[162:163], off
	v_lshl_add_u64 v[162:163], s[58:59], 0, v[148:149]
	s_mov_b32 m0, s18
	s_nop 0
	global_load_lds_dwordx4 v[162:163], off
	v_lshl_add_u64 v[162:163], s[58:59], 0, v[152:153]
	s_add_i32 m0, s18, 0x2000
	s_nop 0
	global_load_lds_dwordx4 v[162:163], off
	v_lshl_add_u64 v[162:163], v[220:221], 0, s[12:13]
	s_mov_b32 m0, s72
	s_nop 0
	global_load_lds_dwordx4 v[162:163], off
	v_lshl_add_u64 v[162:163], v[222:223], 0, s[12:13]
	s_mov_b32 m0, s73
	s_nop 0
	global_load_lds_dwordx4 v[162:163], off
	s_waitcnt vmcnt(8)
	s_waitcnt lgkmcnt(0)
	s_barrier
	s_setprio 1
	s_waitcnt lgkmcnt(0)
	v_mfma_f32_16x16x32_bf16 v[62:65], v[130:133], v[186:189], v[62:65]
	v_mfma_f32_16x16x32_bf16 v[58:61], v[138:141], v[186:189], v[58:61]
	v_mfma_f32_16x16x32_bf16 v[50:53], v[130:133], v[194:197], v[50:53]
	v_mfma_f32_16x16x32_bf16 v[42:45], v[138:141], v[194:197], v[42:45]
	v_mfma_f32_16x16x32_bf16 v[34:37], v[130:133], v[202:205], v[34:37]
	v_mfma_f32_16x16x32_bf16 v[26:29], v[138:141], v[202:205], v[26:29]
	v_mfma_f32_16x16x32_bf16 v[18:21], v[130:133], v[210:213], v[18:21]
	v_mfma_f32_16x16x32_bf16 v[10:13], v[138:141], v[210:213], v[10:13]
	v_mfma_f32_16x16x32_bf16 v[62:65], v[134:137], v[190:193], v[62:65]
	v_mfma_f32_16x16x32_bf16 v[58:61], v[142:145], v[190:193], v[58:61]
	v_mfma_f32_16x16x32_bf16 v[50:53], v[134:137], v[198:201], v[50:53]
	v_mfma_f32_16x16x32_bf16 v[42:45], v[142:145], v[198:201], v[42:45]
	v_mfma_f32_16x16x32_bf16 v[34:37], v[134:137], v[206:209], v[34:37]
	v_mfma_f32_16x16x32_bf16 v[26:29], v[142:145], v[206:209], v[26:29]
	v_mfma_f32_16x16x32_bf16 v[18:21], v[134:137], v[214:217], v[18:21]
	v_mfma_f32_16x16x32_bf16 v[10:13], v[142:145], v[214:217], v[10:13]
	s_setprio 0
	s_setprio 1
	v_mfma_f32_16x16x32_bf16 v[54:57], v[170:173], v[186:189], v[54:57]
	v_mfma_f32_16x16x32_bf16 v[46:49], v[178:181], v[186:189], v[46:49]
	v_mfma_f32_16x16x32_bf16 v[38:41], v[170:173], v[194:197], v[38:41]
	v_mfma_f32_16x16x32_bf16 v[30:33], v[178:181], v[194:197], v[30:33]
	v_mfma_f32_16x16x32_bf16 v[22:25], v[170:173], v[202:205], v[22:25]
	v_mfma_f32_16x16x32_bf16 v[14:17], v[178:181], v[202:205], v[14:17]
	v_mfma_f32_16x16x32_bf16 v[6:9], v[170:173], v[210:213], v[6:9]
	v_mfma_f32_16x16x32_bf16 v[2:5], v[178:181], v[210:213], v[2:5]
	v_mfma_f32_16x16x32_bf16 v[54:57], v[174:177], v[190:193], v[54:57]
	v_mfma_f32_16x16x32_bf16 v[46:49], v[182:185], v[190:193], v[46:49]
	v_mfma_f32_16x16x32_bf16 v[38:41], v[174:177], v[198:201], v[38:41]
	v_mfma_f32_16x16x32_bf16 v[30:33], v[182:185], v[198:201], v[30:33]
	v_mfma_f32_16x16x32_bf16 v[22:25], v[174:177], v[206:209], v[22:25]
	v_mfma_f32_16x16x32_bf16 v[14:17], v[182:185], v[206:209], v[14:17]
	v_mfma_f32_16x16x32_bf16 v[6:9], v[174:177], v[214:217], v[6:9]
	v_mfma_f32_16x16x32_bf16 v[2:5], v[182:185], v[214:217], v[2:5]
	s_setprio 0
	s_add_i32 s86, s86, 2
	s_add_u32 s56, s56, 0x100
	s_addc_u32 s57, s57, 0
	s_add_u32 s84, s84, 0x100
	s_addc_u32 s85, s85, 0
	s_cmp_gt_u32 s86, 29
	s_barrier
	s_cbranch_scc0 .LBB0_927
	s_and_b64 vcc, exec, s[14:15]
	s_cbranch_vccz .LBB0_930
	s_barrier

.LBB0_1171:
	s_add_i32 s95, s95, 2
	s_add_u32 s58, s58, 0x100
	s_addc_u32 s59, s59, 0
	s_add_u32 s92, s92, 0x100
	s_addc_u32 s93, s93, 0
	s_cmp_gt_u32 s95, 13
	s_barrier
	s_cbranch_scc1 .LBB0_1180

.LBB0_1295:
	s_add_i32 s69, s69, 2
	s_add_u32 s64, s64, 0x100
	s_addc_u32 s65, s65, 0
	s_cmp_gt_u32 s69, 13
	v_lshl_add_u64 v[220:221], v[220:221], 0, s[52:53]
	s_barrier
	s_cbranch_scc1 .LBB0_1304
